# router-weight staging in norm2/route: 4-iteration load-wait loop unrolled, 8 loads in flight per chunk
# speedup vs baseline: 1.0093x; 1.0014x over previous
; #define LAS __attribute__((address_space(3)))
; __device__ __forceinline__ unsigned cvtpk(float lo, float hi) { f32x2_t v = {lo, hi}; bf16x2_t b = __builtin_convertvector(v, bf16x2_t); return __builtin_bit_cast(unsigned, b); }
; __device__ __forceinline__ float wave_sum(float v) { v += dppf<DPP_XOR1>(v); v += dppf<DPP_XOR2>(v); v += dppf<DPP_XOR7>(v); v += dppf<DPP_XOR8>(v); return xrow_sum(v); }
; __device__ __forceinline__ void phase_norm2_route(const Ptrs& p, LAS unsigned char* lds) {
;     ...
;             for (int q = 0; q < 2; ++q) { const int row = blk * 32 + half * 16 + wid * 2 + q; const float* xr = x1 + (size_t)row * D; float ss = 0.f;
; #pragma unroll
;                 for (int c = 0; c < 8; ++c) { v[q][c] = __builtin_nontemporal_load((const f32x4*)(xr + c * 256 + lane * 4)); ss += v[q][c][0] * v[q][c][0] + v[q][c][1] * v[q][c][1] + v[q][c][2] * v[q][c][2] + v[q][c][3] * v[q][c][3]; }
;                 ss = wave_sum(ss); const float r = rsqrtf(ss * (1.0f / D) + EPS);
; #pragma unroll
;                 for (int c = 0; c < 8; ++c) { const int k = c * 256 + lane * 4; const f32x4 g4 = *(const LAS f32x4*)(gs + k), s4 = *(const LAS f32x4*)(sh + k);
;                     v[q][c] = (v[q][c] * r) * g4 + s4; u32x2 w; w.x = cvtpk(v[q][c][0], v[q][c][1]); w.y = cvtpk(v[q][c][2], v[q][c][3]); *(u32x2*)(ha + (size_t)row * D + k) = w; } }
.LBB0_925:
	v_lshl_add_u32 v120, s28, 4, v83
	v_ashrrev_i32_e32 v121, 31, v120
	v_lshlrev_b64 v[2:3], 13, v[120:121]
	v_lshl_add_u64 v[2:3], v[74:75], 0, v[2:3]
	global_load_dwordx4 v[42:45], v[2:3], off nt
	global_load_dwordx4 v[46:49], v[2:3], off offset:1024 nt
	global_load_dwordx4 v[50:53], v[2:3], off offset:2048 nt
	global_load_dwordx4 v[54:57], v[2:3], off offset:3072 nt
	v_add_co_u32_e32 v2, vcc, s64, v2
	v_lshlrev_b64 v[92:93], 12, v[120:121]
	s_nop 0
	v_addc_co_u32_e32 v3, vcc, 0, v3, vcc
	global_load_dwordx4 v[58:61], v[2:3], off nt
	global_load_dwordx4 v[62:65], v[2:3], off offset:1024 nt
	global_load_dwordx4 v[88:91], v[2:3], off offset:2048 nt
	global_load_dwordx4 v[66:69], v[2:3], off offset:3072 nt
	ds_read_b128 v[2:5], v158
	ds_read_b128 v[6:9], v159
	ds_read_b128 v[10:13], v160
	ds_read_b128 v[14:17], v161
	ds_read_b128 v[18:21], v162
	ds_read_b128 v[22:25], v163
	ds_read_b128 v[26:29], v164
	ds_read_b128 v[30:33], v165
	v_lshl_add_u64 v[122:123], v[86:87], 0, v[92:93]
	v_or_b32_e32 v124, 1, v120
	v_ashrrev_i32_e32 v125, 31, v124
	v_lshlrev_b64 v[120:121], 13, v[124:125]
	v_lshl_add_u64 v[134:135], v[74:75], 0, v[120:121]
	v_lshlrev_b64 v[124:125], 12, v[124:125]
	v_lshl_add_u64 v[208:209], v[86:87], 0, v[124:125]
	s_waitcnt vmcnt(7)
	v_mul_f32_e32 v34, v43, v43
	s_waitcnt vmcnt(6)
	v_mul_f32_e32 v35, v47, v47
	s_waitcnt vmcnt(5)
	v_mul_f32_e32 v36, v51, v51
	v_fmac_f32_e32 v34, v42, v42
	v_fmac_f32_e32 v35, v46, v46
	s_waitcnt vmcnt(4)
	v_mul_f32_e32 v37, v55, v55
	v_fmac_f32_e32 v36, v50, v50
	v_fmac_f32_e32 v34, v44, v44
	v_fmac_f32_e32 v35, v48, v48
	v_fmac_f32_e32 v37, v54, v54
	s_waitcnt vmcnt(3)
	v_mul_f32_e32 v38, v59, v59
	v_fmac_f32_e32 v36, v52, v52
	v_fmac_f32_e32 v34, v45, v45
	v_fmac_f32_e32 v35, v49, v49
	s_waitcnt vmcnt(2)
	v_mul_f32_e32 v39, v63, v63
	v_fmac_f32_e32 v37, v56, v56
	v_fmac_f32_e32 v38, v58, v58
	v_fmac_f32_e32 v36, v53, v53
	v_add_f32_e32 v34, v34, v35
	s_waitcnt vmcnt(1)
	v_mul_f32_e32 v40, v89, v89
	v_fmac_f32_e32 v39, v62, v62
	v_fmac_f32_e32 v37, v57, v57
	v_fmac_f32_e32 v38, v60, v60
	v_add_f32_e32 v34, v34, v36
	s_waitcnt vmcnt(0)
	v_mul_f32_e32 v41, v67, v67
	v_fmac_f32_e32 v40, v88, v88
	v_fmac_f32_e32 v39, v64, v64
	v_fmac_f32_e32 v38, v61, v61
	v_add_f32_e32 v34, v34, v37
	v_fmac_f32_e32 v41, v66, v66
	v_fmac_f32_e32 v40, v90, v90
	v_fmac_f32_e32 v39, v65, v65
	v_add_f32_e32 v34, v34, v38
	v_fmac_f32_e32 v41, v68, v68
	v_fmac_f32_e32 v40, v91, v91
	v_add_f32_e32 v34, v34, v39
	v_fmac_f32_e32 v41, v69, v69
	v_add_f32_e32 v34, v34, v40
	v_add_f32_e32 v34, v34, v41
	s_nop 1
	v_add_f32_dpp v34, v34, v34 quad_perm:[1,0,3,2] row_mask:0xf bank_mask:0xf bound_ctrl:1
	s_nop 1
	v_add_f32_dpp v34, v34, v34 quad_perm:[2,3,0,1] row_mask:0xf bank_mask:0xf bound_ctrl:1
	s_nop 1
	v_add_f32_dpp v34, v34, v34 row_half_mirror row_mask:0xf bank_mask:0xf bound_ctrl:1
	s_nop 1
	v_add_f32_dpp v34, v34, v34 row_ror:8 row_mask:0xf bank_mask:0xf bound_ctrl:1
	v_mov_b32_e32 v35, v34
	s_nop 1
	v_permlane16_swap_b32_e32 v34, v35
	v_add_f32_e32 v34, v34, v35
	v_mov_b32_e32 v35, v34
	s_nop 1
	v_permlane32_swap_b32_e32 v34, v35
	v_add_f32_e32 v34, v34, v35
	v_fmamk_f32 v34, v34, 0x3a000000, v179
	v_mul_f32_e32 v35, 0x4b800000, v34
	v_cmp_gt_f32_e32 vcc, s69, v34
	s_nop 1
	v_cndmask_b32_e32 v34, v34, v35, vcc
	v_rsq_f32_e32 v72, v34
	ds_read_b128 v[34:37], v166
	ds_read_b128 v[38:41], v167
	v_mul_f32_e32 v92, 0x45800000, v72
	v_cndmask_b32_e32 v72, v72, v92, vcc
	v_pk_mul_f32 v[42:43], v[42:43], v[72:73] op_sel_hi:[1,0]
	v_pk_mul_f32 v[44:45], v[44:45], v[72:73] op_sel_hi:[1,0]
	v_pk_mul_f32 v[46:47], v[46:47], v[72:73] op_sel_hi:[1,0]
	v_pk_mul_f32 v[48:49], v[48:49], v[72:73] op_sel_hi:[1,0]
	v_pk_mul_f32 v[50:51], v[50:51], v[72:73] op_sel_hi:[1,0]
	v_pk_mul_f32 v[52:53], v[52:53], v[72:73] op_sel_hi:[1,0]
	v_pk_mul_f32 v[54:55], v[54:55], v[72:73] op_sel_hi:[1,0]
	v_pk_mul_f32 v[56:57], v[56:57], v[72:73] op_sel_hi:[1,0]
	s_waitcnt lgkmcnt(8)
	v_pk_fma_f32 v[140:141], v[4:5], v[44:45], v[8:9]
	v_pk_fma_f32 v[142:143], v[2:3], v[42:43], v[6:7]
	s_waitcnt lgkmcnt(6)
	v_pk_fma_f32 v[126:127], v[12:13], v[48:49], v[16:17]
	v_pk_fma_f32 v[132:133], v[10:11], v[46:47], v[14:15]
	s_waitcnt lgkmcnt(4)
	v_pk_fma_f32 v[116:117], v[20:21], v[52:53], v[24:25]
	v_pk_fma_f32 v[118:119], v[18:19], v[50:51], v[22:23]
	s_waitcnt lgkmcnt(2)
	v_pk_fma_f32 v[108:109], v[28:29], v[56:57], v[32:33]
	v_pk_fma_f32 v[110:111], v[26:27], v[54:55], v[30:31]
	v_cvt_pk_bf16_f32 v136, v142, v143
	v_cvt_pk_bf16_f32 v137, v140, v141
	v_cvt_pk_bf16_f32 v138, v132, v133
	v_cvt_pk_bf16_f32 v139, v126, v127
	v_cvt_pk_bf16_f32 v112, v118, v119
	v_cvt_pk_bf16_f32 v113, v116, v117
	v_cvt_pk_bf16_f32 v114, v110, v111
	v_cvt_pk_bf16_f32 v115, v108, v109
	global_store_dwordx2 v[122:123], v[136:137], off
	global_store_dwordx2 v[122:123], v[138:139], off offset:512
	global_store_dwordx2 v[122:123], v[112:113], off offset:1024
	global_store_dwordx2 v[122:123], v[114:115], off offset:1536
	ds_read_b128 v[42:45], v168
	ds_read_b128 v[46:49], v169
	v_pk_mul_f32 v[58:59], v[58:59], v[72:73] op_sel_hi:[1,0]
	v_pk_mul_f32 v[60:61], v[60:61], v[72:73] op_sel_hi:[1,0]
	s_waitcnt lgkmcnt(2)
	v_pk_fma_f32 v[100:101], v[34:35], v[58:59], v[38:39]
	v_pk_fma_f32 v[98:99], v[36:37], v[60:61], v[40:41]
	v_cvt_pk_bf16_f32 v96, v100, v101
	v_cvt_pk_bf16_f32 v97, v98, v99
	global_store_dwordx2 v[122:123], v[96:97], off offset:2048
	v_pk_mul_f32 v[50:51], v[62:63], v[72:73] op_sel_hi:[1,0]
	v_pk_mul_f32 v[52:53], v[64:65], v[72:73] op_sel_hi:[1,0]
	s_waitcnt lgkmcnt(0)
; #define LAS __attribute__((address_space(3)))
; __device__ __forceinline__ unsigned cvtpk(float lo, float hi) { f32x2_t v = {lo, hi}; bf16x2_t b = __builtin_convertvector(v, bf16x2_t); return __builtin_bit_cast(unsigned, b); }
; __device__ __forceinline__ float wave_sum(float v) { v += dppf<DPP_XOR1>(v); v += dppf<DPP_XOR2>(v); v += dppf<DPP_XOR7>(v); v += dppf<DPP_XOR8>(v); return xrow_sum(v); }
; __device__ __forceinline__ void phase_norm2_route(const Ptrs& p, LAS unsigned char* lds) {
;     ...
;             for (int q = 0; q < 2; ++q) { const int row = blk * 32 + half * 16 + wid * 2 + q; const float* xr = x1 + (size_t)row * D; float ss = 0.f;
; #pragma unroll
;                 for (int c = 0; c < 8; ++c) { v[q][c] = __builtin_nontemporal_load((const f32x4*)(xr + c * 256 + lane * 4)); ss += v[q][c][0] * v[q][c][0] + v[q][c][1] * v[q][c][1] + v[q][c][2] * v[q][c][2] + v[q][c][3] * v[q][c][3]; }
;                 ss = wave_sum(ss); const float r = rsqrtf(ss * (1.0f / D) + EPS);
; #pragma unroll
;                 for (int c = 0; c < 8; ++c) { const int k = c * 256 + lane * 4; const f32x4 g4 = *(const LAS f32x4*)(gs + k), s4 = *(const LAS f32x4*)(sh + k);
;                     v[q][c] = (v[q][c] * r) * g4 + s4; u32x2 w; w.x = cvtpk(v[q][c][0], v[q][c][1]); w.y = cvtpk(v[q][c][2], v[q][c][3]); *(u32x2*)(ha + (size_t)row * D + k) = w; } }
	v_pk_fma_f32 v[106:107], v[50:51], v[42:43], v[46:47]
	v_pk_fma_f32 v[104:105], v[52:53], v[44:45], v[48:49]
	ds_read_b128 v[50:53], v170
	ds_read_b128 v[54:57], v171
	v_cvt_pk_bf16_f32 v102, v106, v107
	v_cvt_pk_bf16_f32 v103, v104, v105
	global_store_dwordx2 v[122:123], v[102:103], off offset:2560
	v_pk_mul_f32 v[58:59], v[88:89], v[72:73] op_sel_hi:[1,0]
	v_pk_mul_f32 v[60:61], v[90:91], v[72:73] op_sel_hi:[1,0]
	s_waitcnt lgkmcnt(0)
	v_pk_fma_f32 v[92:93], v[58:59], v[50:51], v[54:55]
	v_pk_fma_f32 v[90:91], v[60:61], v[52:53], v[56:57]
	ds_read_b128 v[58:61], v172
	ds_read_b128 v[62:65], v173
	v_pk_mul_f32 v[66:67], v[66:67], v[72:73] op_sel_hi:[1,0]
	v_pk_mul_f32 v[68:69], v[68:69], v[72:73] op_sel_hi:[1,0]
	v_cvt_pk_bf16_f32 v88, v92, v93
	v_cvt_pk_bf16_f32 v89, v90, v91
	s_waitcnt lgkmcnt(0)
	v_pk_fma_f32 v[68:69], v[68:69], v[60:61], v[64:65]
	v_pk_fma_f32 v[94:95], v[66:67], v[58:59], v[62:63]
	v_cvt_pk_bf16_f32 v67, v68, v69
	v_cvt_pk_bf16_f32 v66, v94, v95
	global_store_dwordx2 v[122:123], v[88:89], off offset:3072
	global_store_dwordx2 v[122:123], v[66:67], off offset:3584
	global_load_dwordx4 v[120:123], v[134:135], off nt
	s_nop 0
	global_load_dwordx4 v[128:131], v[134:135], off offset:1024 nt
	global_load_dwordx4 v[184:187], v[134:135], off offset:2048 nt
	global_load_dwordx4 v[188:191], v[134:135], off offset:3072 nt
	v_add_co_u32_e32 v134, vcc, s64, v134
	s_waitcnt vmcnt(3)
	v_mul_f32_e32 v72, v121, v121
	v_addc_co_u32_e32 v135, vcc, 0, v135, vcc
	global_load_dwordx4 v[192:195], v[134:135], off nt
	global_load_dwordx4 v[196:199], v[134:135], off offset:1024 nt
	global_load_dwordx4 v[200:203], v[134:135], off offset:2048 nt
	global_load_dwordx4 v[204:207], v[134:135], off offset:3072 nt
	s_waitcnt vmcnt(6)
	v_mul_f32_e32 v134, v129, v129
	s_waitcnt vmcnt(5)
	v_mul_f32_e32 v135, v185, v185
	v_fmac_f32_e32 v72, v120, v120
	v_fmac_f32_e32 v134, v128, v128
	s_waitcnt vmcnt(4)
	v_mul_f32_e32 v144, v189, v189
	v_fmac_f32_e32 v135, v184, v184
	v_fmac_f32_e32 v72, v122, v122
	v_fmac_f32_e32 v134, v130, v130
	v_fmac_f32_e32 v144, v188, v188
	v_fmac_f32_e32 v135, v186, v186
	v_fmac_f32_e32 v72, v123, v123
	v_fmac_f32_e32 v134, v131, v131
	v_fmac_f32_e32 v144, v190, v190
	v_fmac_f32_e32 v135, v187, v187
	v_add_f32_e32 v72, v72, v134
	v_fmac_f32_e32 v144, v191, v191
	v_add_f32_e32 v72, v72, v135
	v_add_f32_e32 v72, v72, v144
	s_waitcnt vmcnt(3)
	v_mul_f32_e32 v145, v193, v193
	s_waitcnt vmcnt(2)
	v_mul_f32_e32 v146, v197, v197
	v_fmac_f32_e32 v145, v192, v192
	s_waitcnt vmcnt(1)
	v_mul_f32_e32 v147, v201, v201
	v_fmac_f32_e32 v146, v196, v196
	v_fmac_f32_e32 v145, v194, v194
	s_waitcnt vmcnt(0)
	v_mul_f32_e32 v183, v205, v205
	v_fmac_f32_e32 v147, v200, v200
	v_fmac_f32_e32 v146, v198, v198
	v_fmac_f32_e32 v145, v195, v195
	v_fmac_f32_e32 v183, v204, v204
	v_fmac_f32_e32 v147, v202, v202
	v_fmac_f32_e32 v146, v199, v199
	v_add_f32_e32 v72, v72, v145
	v_fmac_f32_e32 v183, v206, v206
	v_fmac_f32_e32 v147, v203, v203
	v_add_f32_e32 v72, v72, v146
	v_fmac_f32_e32 v183, v207, v207
	v_add_f32_e32 v72, v72, v147
	v_add_f32_e32 v72, v72, v183
	s_nop 1
	v_add_f32_dpp v72, v72, v72 quad_perm:[1,0,3,2] row_mask:0xf bank_mask:0xf bound_ctrl:1
	s_nop 1
	v_add_f32_dpp v72, v72, v72 quad_perm:[2,3,0,1] row_mask:0xf bank_mask:0xf bound_ctrl:1
	s_nop 1
	v_add_f32_dpp v72, v72, v72 row_half_mirror row_mask:0xf bank_mask:0xf bound_ctrl:1
	s_nop 1
	v_add_f32_dpp v72, v72, v72 row_ror:8 row_mask:0xf bank_mask:0xf bound_ctrl:1
	v_mov_b32_e32 v134, v72
	s_nop 1
	v_permlane16_swap_b32_e32 v72, v134
	v_add_f32_e32 v72, v72, v134
	v_mov_b32_e32 v134, v72
	s_nop 1
	v_permlane32_swap_b32_e32 v72, v134
	v_add_f32_e32 v72, v72, v134
	v_fmamk_f32 v72, v72, 0x3a000000, v179
	v_mul_f32_e32 v134, 0x4b800000, v72
	v_cmp_gt_f32_e32 vcc, s69, v72
	s_nop 1
	v_cndmask_b32_e32 v72, v72, v134, vcc
	v_rsq_f32_e32 v72, v72
	s_nop 0
	v_mul_f32_e32 v124, 0x45800000, v72
	v_cndmask_b32_e32 v72, v72, v124, vcc
	v_pk_mul_f32 v[122:123], v[122:123], v[72:73] op_sel_hi:[1,0]
	v_pk_mul_f32 v[120:121], v[120:121], v[72:73] op_sel_hi:[1,0]
	v_pk_fma_f32 v[8:9], v[4:5], v[122:123], v[8:9]
	v_pk_mul_f32 v[4:5], v[130:131], v[72:73] op_sel_hi:[1,0]
	v_pk_mul_f32 v[124:125], v[128:129], v[72:73] op_sel_hi:[1,0]
	v_pk_fma_f32 v[146:147], v[2:3], v[120:121], v[6:7]
	v_pk_fma_f32 v[6:7], v[12:13], v[4:5], v[16:17]
	v_pk_mul_f32 v[12:13], v[186:187], v[72:73] op_sel_hi:[1,0]
	v_pk_fma_f32 v[144:145], v[10:11], v[124:125], v[14:15]
	v_pk_mul_f32 v[10:11], v[184:185], v[72:73] op_sel_hi:[1,0]
	v_pk_fma_f32 v[128:129], v[20:21], v[12:13], v[24:25]
	v_pk_mul_f32 v[12:13], v[190:191], v[72:73] op_sel_hi:[1,0]
	v_pk_fma_f32 v[134:135], v[18:19], v[10:11], v[22:23]
	v_pk_mul_f32 v[10:11], v[188:189], v[72:73] op_sel_hi:[1,0]
	v_pk_fma_f32 v[124:125], v[28:29], v[12:13], v[32:33]
	v_pk_mul_f32 v[12:13], v[194:195], v[72:73] op_sel_hi:[1,0]
	v_pk_fma_f32 v[130:131], v[26:27], v[10:11], v[30:31]
	v_pk_mul_f32 v[10:11], v[192:193], v[72:73] op_sel_hi:[1,0]
	v_pk_fma_f32 v[28:29], v[36:37], v[12:13], v[40:41]
	v_pk_mul_f32 v[12:13], v[198:199], v[72:73] op_sel_hi:[1,0]
	v_pk_fma_f32 v[32:33], v[34:35], v[10:11], v[38:39]
	v_pk_mul_f32 v[10:11], v[196:197], v[72:73] op_sel_hi:[1,0]
	v_pk_fma_f32 v[26:27], v[44:45], v[12:13], v[48:49]
	v_pk_mul_f32 v[12:13], v[202:203], v[72:73] op_sel_hi:[1,0]
	v_pk_fma_f32 v[30:31], v[42:43], v[10:11], v[46:47]
	v_pk_mul_f32 v[10:11], v[200:201], v[72:73] op_sel_hi:[1,0]
	v_pk_fma_f32 v[16:17], v[52:53], v[12:13], v[56:57]
	v_pk_mul_f32 v[12:13], v[204:205], v[72:73] op_sel_hi:[1,0]
	v_pk_mul_f32 v[14:15], v[206:207], v[72:73] op_sel_hi:[1,0]
	v_pk_fma_f32 v[20:21], v[50:51], v[10:11], v[54:55]
	v_pk_fma_f32 v[14:15], v[60:61], v[14:15], v[64:65]
	v_pk_fma_f32 v[18:19], v[58:59], v[12:13], v[62:63]
	v_cvt_pk_bf16_f32 v2, v146, v147
	v_cvt_pk_bf16_f32 v3, v8, v9
	v_cvt_pk_bf16_f32 v4, v144, v145
	v_cvt_pk_bf16_f32 v5, v6, v7
	v_cvt_pk_bf16_f32 v120, v134, v135
	v_cvt_pk_bf16_f32 v121, v128, v129
	v_cvt_pk_bf16_f32 v122, v130, v131
	v_cvt_pk_bf16_f32 v123, v124, v125
	v_cvt_pk_bf16_f32 v22, v32, v33
	v_cvt_pk_bf16_f32 v23, v28, v29
	v_cvt_pk_bf16_f32 v24, v30, v31
	v_cvt_pk_bf16_f32 v25, v26, v27
	v_cvt_pk_bf16_f32 v10, v20, v21
	v_cvt_pk_bf16_f32 v11, v16, v17
	v_cvt_pk_bf16_f32 v12, v18, v19
	v_cvt_pk_bf16_f32 v13, v14, v15
	global_store_dwordx2 v[208:209], v[2:3], off
	global_store_dwordx2 v[208:209], v[4:5], off offset:512
	global_store_dwordx2 v[208:209], v[120:121], off offset:1024
	global_store_dwordx2 v[208:209], v[122:123], off offset:1536
	global_store_dwordx2 v[208:209], v[22:23], off offset:2048
	global_store_dwordx2 v[208:209], v[24:25], off offset:2560
	global_store_dwordx2 v[208:209], v[10:11], off offset:3072
	global_store_dwordx2 v[208:209], v[12:13], off offset:3584
	s_barrier
; #define LAS __attribute__((address_space(3)))
; __device__ __forceinline__ unsigned cvtpk(float lo, float hi) { f32x2_t v = {lo, hi}; bf16x2_t b = __builtin_convertvector(v, bf16x2_t); return __builtin_bit_cast(unsigned, b); }
; __device__ __forceinline__ float bflo(unsigned w) { return __uint_as_float(w << 16); }
; __device__ __forceinline__ float bfhi(unsigned w) { return __uint_as_float(w & 0xffff0000u); }
; __device__ __forceinline__ void phase_norm2_route(const Ptrs& p, LAS unsigned char* lds) {
;     ...
;                 for (int i = tid; i < 2048; i += 512) { const int kp = i >> 3, cq = i & 7; const float* w = p.router_w + (size_t)(512 * ch + 2 * kp) * E + cq * 4;
;                     const f32x4 w0 = *(const f32x4*)w, w1 = *(const f32x4*)(w + E);
; #pragma unroll
;                     for (int j = 0; j < 4; ++j) { const unsigned hi = cvtpk(w0[j], w1[j]), lo = cvtpk(w0[j] - bflo(hi), w1[j] - bfhi(hi));
;                         *(LAS unsigned*)(lds + R_WHI + (cq * 4 + j) * R_PITCH + kp * 4) = hi; *(LAS unsigned*)(lds + R_WLO + (cq * 4 + j) * R_PITCH + kp * 4) = lo; } }
	s_and_saveexec_b64 s[46:47], s[4:5]
	s_cbranch_execz .LBB0_928
	v_mov_b32_e32 v34, v151
	v_mov_b32_e32 v35, v70
	v_ashrrev_i32_e32 v44, 3, v35
	v_lshlrev_b32_e32 v36, 1, v44
	v_ashrrev_i32_e32 v37, 31, v36
	v_and_b32_e32 v45, 28, v34
	v_lshlrev_b64 v[36:37], 7, v[36:37]
	v_lshlrev_b32_e32 v72, 2, v45
	v_lshl_add_u64 v[36:37], s[44:45], 0, v[36:37]
	v_lshl_add_u64 v[216:217], v[36:37], 0, v[72:73]
	v_lshlrev_b32_e32 v44, 2, v44
	v_mul_u32_u24_e32 v45, 0x410, v45
	v_add3_u32 v52, 0, v44, v45
	global_load_dwordx4 v[36:39], v[216:217], off
	global_load_dwordx4 v[40:43], v[216:217], off offset:128
	v_add_co_u32_e32 v218, vcc, 0x4000, v216
	s_nop 1
	v_addc_co_u32_e32 v219, vcc, 0, v217, vcc
	global_load_dwordx4 v[220:223], v[218:219], off
	global_load_dwordx4 v[224:227], v[218:219], off offset:128
	v_add_co_u32_e32 v218, vcc, 0x8000, v216
	s_nop 1
	v_addc_co_u32_e32 v219, vcc, 0, v217, vcc
	global_load_dwordx4 v[228:231], v[218:219], off
	global_load_dwordx4 v[232:235], v[218:219], off offset:128
	v_add_co_u32_e32 v218, vcc, 0xc000, v216
	s_nop 1
	v_addc_co_u32_e32 v219, vcc, 0, v217, vcc
	global_load_dwordx4 v[236:239], v[218:219], off
	global_load_dwordx4 v[240:243], v[218:219], off offset:128
	s_waitcnt vmcnt(0)
	v_cvt_pk_bf16_f32 v46, v36, v40
	v_cvt_pk_bf16_f32 v47, v37, v41
	v_cvt_pk_bf16_f32 v48, v38, v42
	v_cvt_pk_bf16_f32 v49, v39, v43
	ds_write_b32 v52, v46
	ds_write_b32 v52, v47 offset:1040
	ds_write_b32 v52, v48 offset:2080
	ds_write_b32 v52, v49 offset:3120
	v_lshlrev_b32_e32 v50, 16, v46
	v_and_b32_e32 v51, 0xffff0000, v46
	v_sub_f32_e32 v50, v36, v50
	v_sub_f32_e32 v51, v40, v51
	v_cvt_pk_bf16_f32 v44, v50, v51
	v_lshlrev_b32_e32 v50, 16, v47
	v_and_b32_e32 v51, 0xffff0000, v47
	v_sub_f32_e32 v50, v37, v50
	v_sub_f32_e32 v51, v41, v51
	v_cvt_pk_bf16_f32 v45, v50, v51
	v_lshlrev_b32_e32 v50, 16, v48
	v_and_b32_e32 v51, 0xffff0000, v48
	v_sub_f32_e32 v50, v38, v50
	v_sub_f32_e32 v51, v42, v51
	v_cvt_pk_bf16_f32 v53, v50, v51
	v_lshlrev_b32_e32 v50, 16, v49
	v_and_b32_e32 v51, 0xffff0000, v49
	v_sub_f32_e32 v50, v39, v50
	v_sub_f32_e32 v51, v43, v51
	v_cvt_pk_bf16_f32 v35, v50, v51
	ds_write_b32 v52, v44 offset:33280
	ds_write_b32 v52, v45 offset:34320
	ds_write_b32 v52, v53 offset:35360
	ds_write_b32 v52, v35 offset:36400
	v_cvt_pk_bf16_f32 v46, v220, v224
	v_cvt_pk_bf16_f32 v47, v221, v225
	v_cvt_pk_bf16_f32 v48, v222, v226
	v_cvt_pk_bf16_f32 v49, v223, v227
	ds_write_b32 v52, v46 offset:256
	ds_write_b32 v52, v47 offset:1296
	ds_write_b32 v52, v48 offset:2336
	ds_write_b32 v52, v49 offset:3376
	v_lshlrev_b32_e32 v50, 16, v46
	v_and_b32_e32 v51, 0xffff0000, v46
	v_sub_f32_e32 v50, v220, v50
	v_sub_f32_e32 v51, v224, v51
	v_cvt_pk_bf16_f32 v44, v50, v51
	v_lshlrev_b32_e32 v50, 16, v47
	v_and_b32_e32 v51, 0xffff0000, v47
	v_sub_f32_e32 v50, v221, v50
	v_sub_f32_e32 v51, v225, v51
	v_cvt_pk_bf16_f32 v45, v50, v51
	v_lshlrev_b32_e32 v50, 16, v48
	v_and_b32_e32 v51, 0xffff0000, v48
	v_sub_f32_e32 v50, v222, v50
	v_sub_f32_e32 v51, v226, v51
	v_cvt_pk_bf16_f32 v53, v50, v51
	v_lshlrev_b32_e32 v50, 16, v49
	v_and_b32_e32 v51, 0xffff0000, v49
	v_sub_f32_e32 v50, v223, v50
	v_sub_f32_e32 v51, v227, v51
	v_cvt_pk_bf16_f32 v35, v50, v51
	ds_write_b32 v52, v44 offset:33536
	ds_write_b32 v52, v45 offset:34576
	ds_write_b32 v52, v53 offset:35616
	ds_write_b32 v52, v35 offset:36656
	v_cvt_pk_bf16_f32 v46, v228, v232
	v_cvt_pk_bf16_f32 v47, v229, v233
	v_cvt_pk_bf16_f32 v48, v230, v234
	v_cvt_pk_bf16_f32 v49, v231, v235
	ds_write_b32 v52, v46 offset:512
	ds_write_b32 v52, v47 offset:1552
	ds_write_b32 v52, v48 offset:2592
	ds_write_b32 v52, v49 offset:3632
	v_lshlrev_b32_e32 v50, 16, v46
	v_and_b32_e32 v51, 0xffff0000, v46
	v_sub_f32_e32 v50, v228, v50
	v_sub_f32_e32 v51, v232, v51
	v_cvt_pk_bf16_f32 v44, v50, v51
	v_lshlrev_b32_e32 v50, 16, v47
	v_and_b32_e32 v51, 0xffff0000, v47
	v_sub_f32_e32 v50, v229, v50
	v_sub_f32_e32 v51, v233, v51
	v_cvt_pk_bf16_f32 v45, v50, v51
	v_lshlrev_b32_e32 v50, 16, v48
	v_and_b32_e32 v51, 0xffff0000, v48
	v_sub_f32_e32 v50, v230, v50
	v_sub_f32_e32 v51, v234, v51
	v_cvt_pk_bf16_f32 v53, v50, v51
	v_lshlrev_b32_e32 v50, 16, v49
	v_and_b32_e32 v51, 0xffff0000, v49
	v_sub_f32_e32 v50, v231, v50
	v_sub_f32_e32 v51, v235, v51
	v_cvt_pk_bf16_f32 v35, v50, v51
	ds_write_b32 v52, v44 offset:33792
	ds_write_b32 v52, v45 offset:34832
	ds_write_b32 v52, v53 offset:35872
	ds_write_b32 v52, v35 offset:36912
	v_cvt_pk_bf16_f32 v46, v236, v240
	v_cvt_pk_bf16_f32 v47, v237, v241
	v_cvt_pk_bf16_f32 v48, v238, v242
	v_cvt_pk_bf16_f32 v49, v239, v243
	ds_write_b32 v52, v46 offset:768
	ds_write_b32 v52, v47 offset:1808
	ds_write_b32 v52, v48 offset:2848
	ds_write_b32 v52, v49 offset:3888
	v_lshlrev_b32_e32 v50, 16, v46
	v_and_b32_e32 v51, 0xffff0000, v46
	v_sub_f32_e32 v50, v236, v50
	v_sub_f32_e32 v51, v240, v51
	v_cvt_pk_bf16_f32 v44, v50, v51
	v_lshlrev_b32_e32 v50, 16, v47
	v_and_b32_e32 v51, 0xffff0000, v47
	v_sub_f32_e32 v50, v237, v50
	v_sub_f32_e32 v51, v241, v51
	v_cvt_pk_bf16_f32 v45, v50, v51
	v_lshlrev_b32_e32 v50, 16, v48
	v_and_b32_e32 v51, 0xffff0000, v48
	v_sub_f32_e32 v50, v238, v50
	v_sub_f32_e32 v51, v242, v51
	v_cvt_pk_bf16_f32 v53, v50, v51
	v_lshlrev_b32_e32 v50, 16, v49
	v_and_b32_e32 v51, 0xffff0000, v49
	v_sub_f32_e32 v50, v239, v50
	v_sub_f32_e32 v51, v243, v51
	v_cvt_pk_bf16_f32 v35, v50, v51
	ds_write_b32 v52, v44 offset:34048
	ds_write_b32 v52, v45 offset:35088
	ds_write_b32 v52, v53 offset:36128
	ds_write_b32 v52, v35 offset:37168
